# same as previous best; code placement of the attention phase and of the phases behind it re-aligned (nop padding executed once per phase)
# baseline (speedup 1.0000x reference)
; #define LAS __attribute__((address_space(3)))
;     __device__ __forceinline__ int vcu() const { return (G % 8 == 0) ? (c % 8) * (G / 8) + c / 8 : c; }
;     __device__ __forceinline__ int vcu() const { return (G % 8 == 0) ? (c % 8) * (G / 8) + c / 8 : c; }
; #define RUN(k, ...) if (IN(k)) { { __VA_ARGS__ } if ((PROBE_DUP_MASK >> (k)) & 1u) { __syncthreads(); { __VA_ARGS__ } } if (BOTH(k)) SEAM(); }
; __device__ __forceinline__ void ph_attn_fast2(const Args& a, LAS unsigned char* lds) {
;     ...
;     const int tid = threadIdx.x, lane = tid & 63, wave = __builtin_amdgcn_readfirstlane(tid >> 6);
;     const int fr = lane & 15, g4 = lane >> 4;
;     int ksrc, vsrc;
;     { int R, C; pg8::stage_rc(wave * 1024 + lane * 16, R, C); ksrc = R * 64 + C;
;       const int key = 8 * wave + (lane >> 3), pos = lane & 7, chunk = (pos >> 1) ^ ((key >> 1) & 3); vsrc = key * 64 + (chunk * 2 + (pos & 1)) * 8; }
;     const int vlane = (4 * g4 + (fr >> 2)) * 128 + (fr & 3) * 8, swz = (2 * g4 + (fr >> 3)) & 3;
;     LAS _Float16* ps = (LAS _Float16*)(lds + AT2_PS + wave * 8192);
;     LAS unsigned* mskl = (LAS unsigned*)(lds + AT2_MSK + wave * 128);
;     const float NEG = -INFINITY;
;     const bf16x8 onesf = (fr == 0) ? (bf16x8){0x3F80, 0x3F80, 0x3F80, 0x3F80, 0x3F80, 0x3F80, 0x3F80, 0x3F80} : (bf16x8){0, 0, 0, 0, 0, 0, 0, 0};
;     const int vcu = (gridDim.x % 8 == 0) ? (int)((blockIdx.x % 8) * (gridDim.x / 8) + blockIdx.x / 8) : (int)blockIdx.x;
; __global__ void __launch_bounds__(512, 2) fwd_kernel(Args a) {
;     ...
;     RUN(15, ph_attn_fast2(a, L);)
.LBB0_1917:
	s_cmp_lt_i32 s58, 16
	s_cselect_b64 s[0:1], -1, 0
	s_cmp_gt_i32 s59, 15
	s_cselect_b64 s[2:3], -1, 0
	s_and_b64 s[0:1], s[0:1], s[2:3]
	s_andn2_b64 vcc, exec, s[0:1]
	s_cbranch_vccnz .LBB0_2342
	s_nop 0
	s_load_dword s1, s[82:83], 0x120
	s_add_u32 s4, s82, 0x120
	s_addc_u32 s5, s83, 0
	v_writelane_b32 v252, s4, 9
	v_readfirstlane_b32 s2, v0
	s_waitcnt lgkmcnt(0)
	s_and_b32 s0, s1, 7
	v_writelane_b32 v252, s5, 10
	s_cmp_lg_u32 s0, 0
	s_mov_b32 s4, s33
	v_writelane_b32 v252, s1, 11
	s_cbranch_scc1 .LBB0_1920
	s_load_dword s1, s[82:83], 0x120
	s_and_b32 s0, s33, 7
	s_waitcnt lgkmcnt(0)
	s_lshr_b32 s1, s1, 3
	s_mul_i32 s0, s1, s0
	s_lshr_b32 s1, s33, 3
	s_add_i32 s4, s0, s1
	s_load_dword s1, s[82:83], 0x120

; __device__ __forceinline__ void xcd_barrier(const XcdBarrier& b) {
;     ...
;             asm volatile("s_waitcnt vmcnt(0)" ::: "memory");
;         }
;     }
;     __syncthreads();
.LBB0_2341:
	s_or_b64 exec, exec, s[0:1]
	s_waitcnt lgkmcnt(0)
	s_barrier
	s_nop 0
	s_nop 0
	s_nop 0
	s_nop 0
	s_nop 0
	s_nop 0
	s_nop 0
	s_nop 0
	s_nop 0
	s_nop 0
	s_nop 0
	s_nop 0
	s_nop 0
	s_nop 0
	s_nop 0
	s_nop 0
	s_nop 0
	s_nop 0
	s_nop 0
	s_nop 0
	s_nop 0
	s_nop 0
	s_nop 0
	s_nop 0
	s_nop 0
	s_nop 0
	s_nop 0
	s_nop 0
	s_nop 0
	s_nop 0
	s_nop 0
	s_nop 0
	s_nop 0
	s_nop 0
	s_nop 0
	s_nop 0
	s_nop 0
	s_nop 0
	s_nop 0
	s_nop 0
	s_nop 0
	s_nop 0
	s_nop 0
	s_nop 0
	s_nop 0
	s_nop 0
	s_nop 0
	s_nop 0
	s_nop 0
	s_nop 0
	s_nop 0
	s_nop 0
	s_nop 0
	s_nop 0
	s_nop 0
	s_nop 0
	s_nop 0
	s_nop 0
	s_nop 0
	s_nop 0
	s_nop 0
	s_nop 0
	s_nop 0
	s_nop 0
	s_nop 0
	s_nop 0
	s_nop 0
	s_nop 0
	s_nop 0
	s_nop 0
	s_nop 0
	s_nop 0
	s_nop 0
	s_nop 0
	s_nop 0
	s_nop 0
	s_nop 0
	s_nop 0
	s_nop 0
	s_nop 0
	s_nop 0
	s_nop 0
	s_nop 0
	s_nop 0
	s_nop 0
	s_nop 0
	s_nop 0
	s_nop 0
	s_nop 0
	s_nop 0
	s_nop 0
	s_nop 0
	s_nop 0
	s_nop 0
	s_nop 0
	s_nop 0
	s_nop 0
	s_nop 0
	s_nop 0
	s_nop 0
	s_nop 0
	s_nop 0
	s_nop 0
	s_nop 0
	s_nop 0
	s_nop 0
	s_nop 0
	s_nop 0
	s_nop 0
	s_nop 0
	s_nop 0
	s_nop 0
	s_nop 0
	s_nop 0
	s_nop 0
	s_nop 0
	s_nop 0
	s_nop 0
	s_nop 0
	s_nop 0
	s_nop 0
	s_nop 0
	s_nop 0
	s_nop 0
	s_nop 0
	s_nop 0
	s_nop 0
	s_nop 0
	s_nop 0
